# vaccH LDS half: weight-word loads use scalar-base addressing (loop + set-up block)
# speedup vs baseline: 1.0031x; 1.0031x over previous
; #define LAS __attribute__((address_space(3)))
; __device__ __forceinline__ unsigned xb_add(unsigned* p, unsigned v) { return __hip_atomic_fetch_add(p, v, __ATOMIC_RELAXED, __HIP_MEMORY_SCOPE_AGENT); }
; __device__ __forceinline__ unsigned xb_xcc_id() { return (unsigned)__builtin_amdgcn_s_getreg((3 << 11) | 20) & 0xFu; }
; __device__ __forceinline__ XcdBarrier xcd_barrier_post(unsigned* bar, volatile LAS unsigned* st) {
;     XcdBarrier b; b.bar = bar; b.x = xb_xcc_id(); b.st = st;
;     if (threadIdx.x == 0) (void)xb_add(&bar[XB_XCNT(b.x)], 1u);
;     return b;
; __global__ void __launch_bounds__(NTHREADS, 2) fwd(Args args) {
;     extern __shared__ __attribute__((aligned(16))) unsigned char lds_raw[];
;     LAS unsigned char* lds = (LAS unsigned char*)lds_raw;
;     const int tid = threadIdx.x, G = gridDim.x, cblk = blockIdx.x;
;     unsigned char* ws = args.ws;
;     volatile LAS unsigned* MISC = (volatile LAS unsigned*)(lds + MISC_OFF);
;     if (tid < 64) MISC[tid] = 0u;
;     __syncthreads();
;     const int lo = args.ph_lo, hi = args.ph_hi;
;     unsigned* barw = (unsigned*)(ws + WS_CTL) + CW_BAR;
;     XcdBarrier bar; bar.bar = barw; bar.x = 0; bar.st = nullptr;
;     if (hi - lo > 1) bar = xcd_barrier_post(barw, MISC + 8);
_Z3fwd4Args:
	v_mov_b32_e32 v239, 3
	s_load_dwordx8 s[84:91], s[0:1], 0x100
	s_load_dwordx2 s[92:93], s[0:1], 0x120
	s_load_dword s34, s[0:1], 0x128
	s_add_u32 s4, s0, 0x128
	s_addc_u32 s5, s1, 0
	v_cmp_gt_u32_e32 vcc, 64, v0
	v_writelane_b32 v227, s4, 0
	s_nop 1
	v_writelane_b32 v227, s5, 1
	s_and_saveexec_b64 s[4:5], vcc
	v_lshl_add_u32 v1, v0, 2, 0
	v_add_u32_e32 v1, 0x20000, v1
	v_mov_b32_e32 v2, 0
	ds_write_b32 v1, v2
	s_or_b64 exec, exec, s[4:5]
	s_load_dwordx16 s[4:19], s[0:1], 0x0
	s_waitcnt lgkmcnt(0)
	s_add_u32 s80, s90, 0x4000
	s_addc_u32 s81, s91, 0
	s_sub_i32 s3, s93, s92
	s_mov_b32 s82, 0
	v_writelane_b32 v227, s4, 2
	s_cmp_lt_i32 s3, 2
	v_cmp_eq_u32_e32 vcc, 0, v0
	v_writelane_b32 v227, s5, 3
	v_writelane_b32 v227, s6, 4
	v_writelane_b32 v227, s7, 5
	v_writelane_b32 v227, s8, 6
	v_writelane_b32 v227, s9, 7
	v_writelane_b32 v227, s10, 8
	v_writelane_b32 v227, s11, 9
	v_writelane_b32 v227, s12, 10
	v_writelane_b32 v227, s13, 11
	v_writelane_b32 v227, s14, 12
	v_writelane_b32 v227, s15, 13
	v_writelane_b32 v227, s16, 14
	v_writelane_b32 v227, s17, 15
	v_writelane_b32 v227, s18, 16
	s_mov_b32 s83, 0
	v_writelane_b32 v227, s19, 17
	s_barrier
	s_cbranch_scc1 .LBB0_7
	s_getreg_b32 s3, hwreg(HW_REG_XCC_ID, 0, 4)
	s_and_b32 s82, s3, 15
	s_and_saveexec_b64 s[4:5], vcc
	s_cbranch_execz .LBB0_6
	s_mov_b64 s[6:7], exec
	v_mbcnt_lo_u32_b32 v1, s6, 0
	v_mbcnt_hi_u32_b32 v1, s7, v1
	v_cmp_eq_u32_e32 vcc, 0, v1
	s_and_b64 s[8:9], exec, vcc
	s_mov_b64 exec, s[8:9]
	s_cbranch_execz .LBB0_6
	s_lshl_b32 s3, s82, 8
	s_bcnt1_i32_b64 s6, s[6:7]
	v_mov_b32_e32 v1, s3
	v_mov_b32_e32 v2, s6
	global_atomic_add v1, v2, s[80:81] offset:1024

; #define VL_LOAD(wr, C) do { _Pragma("unroll") for (int i = 0; i < 16; ++i) wr[i] = wp[(size_t)((C) * 16 + i) * MROWS]; } while (0)
; #define VL_LOAD(wr, C) do { _Pragma("unroll") for (int i = 0; i < 16; ++i) wr[i] = wp[(size_t)((C) * 16 + i) * MROWS]; } while (0)
; template <bool RUN_L = true, bool RUN_G = true, bool DRY = false>
; __device__ __forceinline__ void phase_vaccH(unsigned char* ws, LAS unsigned char* lds, int layer, int G) {
;     ...
;             for (int tb = wid; tb < NTB; tb += 4) {
;                 const int tok = tb * 64 + lane; const bool valid = tok < MROWS; const int tokc = valid ? tok : MROWS - 1;
;                 const unsigned* wp = WLT + tokc;
;                 f32x4* hp = (f32x4*)(H + (size_t)tokc * D + cg * 8); const f32x4 h0 = hp[0], h1 = hp[1];
;                 float accf[8];
; #pragma unroll
;                 for (int j = 0; j < 8; ++j) accf[j] = 0.f;
;                 unsigned wa[16], wb[16];
;                 VL_LOAD(wa, 0);
; #pragma unroll 1
;                 for (int c = 0; c < 8; c += 2) {
;                     VL_LOAD(wb, c + 1);
.LBB0_1241:
	s_waitcnt vmcnt(1)
	v_lshl_or_b32 v2, s29, 6, v1
	s_movk_i32 s6, 0x2010
	v_cmp_gt_i32_e64 s[6:7], s6, v2
	v_mov_b32_e32 v28, 0
	s_mov_b32 s46, 32
	v_cndmask_b32_e64 v12, v171, v2, s[6:7]
	v_ashrrev_i32_e32 v13, 31, v12
	v_lshlrev_b64 v[14:15], 2, v[12:13]
	v_mov_b32_e32 v238, v14
	v_lshlrev_b64 v[2:3], 14, v[12:13]
	v_lshl_add_u64 v[12:13], s[16:17], 0, v[14:15]
	v_lshl_add_u64 v[10:11], s[30:31], 0, v[2:3]
	global_load_dwordx4 v[2:5], v[10:11], off offset:16
	global_load_dwordx4 v[6:9], v[10:11], off
	global_load_dword v36, v238, s[16:17]
	s_add_u32 s78, s16, s62
	s_addc_u32 s79, s17, 0
	global_load_dword v37, v238, s[78:79] offset:64
	v_lshl_add_u64 v[14:15], s[18:19], 0, v[14:15]
	s_mov_b64 s[76:77], s[18:19]
	s_add_u32 s78, s16, s56
	s_addc_u32 s79, s17, 0
	global_load_dword v38, v238, s[78:79] offset:128
	s_mov_b32 s47, -2
	s_add_u32 s78, s16, s57
	s_addc_u32 s79, s17, 0
	global_load_dword v39, v238, s[78:79] offset:192
	v_mov_b32_e32 v29, v28
	s_add_u32 s78, s16, s64
	s_addc_u32 s79, s17, 0
	global_load_dword v40, v238, s[78:79] offset:256
	v_mov_b32_e32 v34, v28
	s_add_u32 s78, s16, s65
	s_addc_u32 s79, s17, 0
	global_load_dword v41, v238, s[78:79] offset:320
	v_mov_b32_e32 v35, v28
	s_add_u32 s78, s16, s66
	s_addc_u32 s79, s17, 0
	global_load_dword v42, v238, s[78:79] offset:384
	v_mov_b32_e32 v22, v28
	s_add_u32 s78, s16, s67
	s_addc_u32 s79, s17, 0
	global_load_dword v44, v238, s[78:79] offset:448
	v_mov_b32_e32 v23, v28
	s_add_u32 s78, s16, s68
	s_addc_u32 s79, s17, 0
	global_load_dword v43, v238, s[78:79] offset:512
	v_mov_b32_e32 v20, v28
	s_add_u32 s78, s16, s69
	s_addc_u32 s79, s17, 0
	global_load_dword v45, v238, s[78:79] offset:576
	v_mov_b32_e32 v21, v28
	s_add_u32 s78, s16, s70
	s_addc_u32 s79, s17, 0
	global_load_dword v46, v238, s[78:79] offset:640
	s_add_u32 s78, s16, s71
	s_addc_u32 s79, s17, 0
	global_load_dword v47, v238, s[78:79] offset:704
	s_add_u32 s78, s16, s72
	s_addc_u32 s79, s17, 0
	global_load_dword v48, v238, s[78:79] offset:768
	s_add_u32 s78, s16, 0x68000
	s_addc_u32 s79, s17, 0
	global_load_dword v49, v238, s[78:79] offset:832
	s_add_u32 s78, s16, 0x70000
	s_addc_u32 s79, s17, 0
	global_load_dword v50, v238, s[78:79] offset:896
	s_add_u32 s78, s16, 0x78000
	s_addc_u32 s79, s17, 0
	global_load_dword v51, v238, s[78:79] offset:960
.LBB0_1242:
	global_load_dword v24, v238, s[76:77]
	s_add_u32 s78, s76, s62
	s_addc_u32 s79, s77, 0
	global_load_dword v31, v238, s[78:79] offset:64
	v_mov_b32_e32 v19, v29
	s_add_u32 s78, s76, s56
	s_addc_u32 s79, s77, 0
	global_load_dword v30, v238, s[78:79] offset:128
	v_mov_b32_e32 v18, v28
	s_add_u32 s78, s76, s57
	s_addc_u32 s79, s77, 0
	global_load_dword v29, v238, s[78:79] offset:192
	v_mov_b32_e32 v17, v35
	s_add_u32 s78, s76, s64
	s_addc_u32 s79, s77, 0
	global_load_dword v28, v238, s[78:79] offset:256
	v_mov_b32_e32 v16, v34
	s_add_u32 s78, s76, s65
	s_addc_u32 s79, s77, 0
	global_load_dword v27, v238, s[78:79] offset:320
	s_add_u32 s78, s76, s66
	s_addc_u32 s79, s77, 0
	global_load_dword v26, v238, s[78:79] offset:384
	s_add_u32 s78, s76, s67
	s_addc_u32 s79, s77, 0
	global_load_dword v25, v238, s[78:79] offset:448
	s_add_u32 s78, s76, s68
	s_addc_u32 s79, s77, 0
	global_load_dword v54, v238, s[78:79] offset:512
	s_add_u32 s78, s76, s69
	s_addc_u32 s79, s77, 0
	global_load_dword v53, v238, s[78:79] offset:576
	s_add_u32 s78, s76, s70
	s_addc_u32 s79, s77, 0
	global_load_dword v52, v238, s[78:79] offset:640
	s_add_u32 s78, s76, s71
	s_addc_u32 s79, s77, 0
	global_load_dword v35, v238, s[78:79] offset:704
	s_add_u32 s78, s76, s72
	s_addc_u32 s79, s77, 0
	global_load_dword v34, v238, s[78:79] offset:768
	s_add_u32 s78, s76, s73
	s_addc_u32 s79, s77, 0
	global_load_dword v33, v238, s[78:79] offset:832
	s_add_u32 s78, s76, s74
	s_addc_u32 s79, s77, 0
	global_load_dword v32, v238, s[78:79] offset:896
	s_add_u32 s78, s76, s75
	s_addc_u32 s79, s77, 0
	global_load_dword v55, v238, s[78:79] offset:960
	s_waitcnt vmcnt(30)
	v_bfe_u32 v57, v37, 16, 16
	v_lshl_add_u32 v58, v57, 3, 0
	s_waitcnt vmcnt(29)
	v_bfe_u32 v57, v38, 16, 16
	v_bfe_u32 v56, v36, 16, 16
	v_lshl_add_u32 v60, v57, 3, 0
	s_waitcnt vmcnt(28)
	v_bfe_u32 v57, v39, 16, 16
	v_lshl_add_u32 v56, v56, 3, 0
	v_lshl_add_u32 v62, v57, 3, 0
	ds_read_b64 v[56:57], v56
	ds_read_b64 v[58:59], v58
	ds_read_b64 v[60:61], v60
	ds_read_b64 v[62:63], v62
	v_perm_b32 v36, v36, v36, s63
	s_waitcnt lgkmcnt(3)
	v_perm_b32 v88, 0, v56, v169
	v_perm_b32 v56, 0, v56, v170
	v_perm_b32 v89, 0, v57, v169
	v_perm_b32 v57, 0, v57, v170
	v_pk_fma_f16 v88, v36, v88, 0
	v_pk_fma_f16 v56, v36, v56, 0
	v_pk_fma_f16 v89, v36, v89, 0
	v_pk_fma_f16 v36, v36, v57, 0
	v_perm_b32 v37, v37, v37, s63
	s_waitcnt lgkmcnt(2)
	v_perm_b32 v57, 0, v58, v169
	v_perm_b32 v58, 0, v58, v170
	v_pk_fma_f16 v56, v37, v58, v56
	v_perm_b32 v58, 0, v59, v169
	v_perm_b32 v59, 0, v59, v170
	v_pk_fma_f16 v57, v37, v57, v88
	v_pk_fma_f16 v58, v37, v58, v89
	v_pk_fma_f16 v36, v37, v59, v36
	v_perm_b32 v37, v38, v38, s63
	s_waitcnt lgkmcnt(1)
	v_perm_b32 v38, 0, v60, v169
	v_pk_fma_f16 v38, v37, v38, v57
	v_perm_b32 v57, 0, v60, v170
	s_waitcnt vmcnt(26)
	v_bfe_u32 v65, v41, 16, 16
	v_pk_fma_f16 v56, v37, v57, v56
	v_perm_b32 v57, 0, v61, v169
	v_lshl_add_u32 v66, v65, 3, 0
	s_waitcnt vmcnt(25)
	v_bfe_u32 v65, v42, 16, 16
	v_pk_fma_f16 v57, v37, v57, v58
	v_perm_b32 v58, 0, v61, v170
	v_bfe_u32 v64, v40, 16, 16
	v_lshl_add_u32 v68, v65, 3, 0
	s_waitcnt vmcnt(24)
	v_bfe_u32 v65, v44, 16, 16
	v_pk_fma_f16 v36, v37, v58, v36
	v_perm_b32 v37, v39, v39, s63
	s_waitcnt lgkmcnt(0)
; #define VL_LOAD(wr, C) do { _Pragma("unroll") for (int i = 0; i < 16; ++i) wr[i] = wp[(size_t)((C) * 16 + i) * MROWS]; } while (0)
; #define VL_LOAD(wr, C) do { _Pragma("unroll") for (int i = 0; i < 16; ++i) wr[i] = wp[(size_t)((C) * 16 + i) * MROWS]; } while (0)
; template <bool RUN_L = true, bool RUN_G = true, bool DRY = false>
; __device__ __forceinline__ void phase_vaccH(unsigned char* ws, LAS unsigned char* lds, int layer, int G) {
;     ...
;                     VL_CHUNK(wa);
;                     __builtin_amdgcn_sched_barrier(0);
;                     VL_LOAD(wa, (c + 2) & 7);
	v_perm_b32 v39, 0, v62, v169
	v_lshl_add_u32 v64, v64, 3, 0
	v_lshl_add_u32 v70, v65, 3, 0
	v_pk_fma_f16 v38, v37, v39, v38
	v_perm_b32 v39, 0, v62, v170
	ds_read_b64 v[64:65], v64
	ds_read_b64 v[66:67], v66
	ds_read_b64 v[68:69], v68
	ds_read_b64 v[70:71], v70
	v_pk_fma_f16 v39, v37, v39, v56
	v_perm_b32 v56, 0, v63, v169
	v_pk_fma_f16 v56, v37, v56, v57
	v_perm_b32 v57, 0, v63, v170
	v_pk_fma_f16 v36, v37, v57, v36
	v_perm_b32 v37, v40, v40, s63
	s_waitcnt lgkmcnt(3)
	v_perm_b32 v40, 0, v64, v169
	v_pk_fma_f16 v38, v37, v40, v38
	v_perm_b32 v40, 0, v64, v170
	v_pk_fma_f16 v39, v37, v40, v39
	v_perm_b32 v40, 0, v65, v169
	v_pk_fma_f16 v40, v37, v40, v56
	v_perm_b32 v56, 0, v65, v170
	v_pk_fma_f16 v36, v37, v56, v36
	v_perm_b32 v37, v41, v41, s63
	s_waitcnt lgkmcnt(2)
	v_perm_b32 v41, 0, v66, v169
	v_pk_fma_f16 v38, v37, v41, v38
	v_perm_b32 v41, 0, v66, v170
	v_pk_fma_f16 v39, v37, v41, v39
	v_perm_b32 v41, 0, v67, v169
	v_pk_fma_f16 v40, v37, v41, v40
	v_perm_b32 v41, 0, v67, v170
	v_pk_fma_f16 v36, v37, v41, v36
	v_perm_b32 v37, v42, v42, s63
	s_waitcnt lgkmcnt(1)
	v_perm_b32 v41, 0, v68, v169
	v_pk_fma_f16 v38, v37, v41, v38
	v_perm_b32 v41, 0, v68, v170
	s_waitcnt vmcnt(22)
	v_bfe_u32 v73, v45, 16, 16
	v_pk_fma_f16 v39, v37, v41, v39
	v_perm_b32 v41, 0, v69, v169
	v_lshl_add_u32 v74, v73, 3, 0
	s_waitcnt vmcnt(21)
	v_bfe_u32 v73, v46, 16, 16
	v_pk_fma_f16 v40, v37, v41, v40
	v_perm_b32 v41, 0, v69, v170
	v_bfe_u32 v72, v43, 16, 16
	v_lshl_add_u32 v76, v73, 3, 0
	s_waitcnt vmcnt(20)
	v_bfe_u32 v73, v47, 16, 16
	v_pk_fma_f16 v36, v37, v41, v36
	v_perm_b32 v37, v44, v44, s63
	s_waitcnt lgkmcnt(0)
	v_perm_b32 v41, 0, v70, v169
	v_lshl_add_u32 v72, v72, 3, 0
	v_lshl_add_u32 v78, v73, 3, 0
	v_pk_fma_f16 v38, v37, v41, v38
	v_perm_b32 v41, 0, v70, v170
	ds_read_b64 v[72:73], v72
	ds_read_b64 v[74:75], v74
	ds_read_b64 v[76:77], v76
	ds_read_b64 v[78:79], v78
	v_pk_fma_f16 v39, v37, v41, v39
	v_perm_b32 v41, 0, v71, v169
	v_pk_fma_f16 v40, v37, v41, v40
	v_perm_b32 v41, 0, v71, v170
	v_pk_fma_f16 v36, v37, v41, v36
	v_perm_b32 v37, v43, v43, s63
	s_waitcnt lgkmcnt(3)
	v_perm_b32 v41, 0, v72, v169
	v_pk_fma_f16 v38, v37, v41, v38
	v_perm_b32 v41, 0, v72, v170
	v_pk_fma_f16 v39, v37, v41, v39
	v_perm_b32 v41, 0, v73, v169
	v_pk_fma_f16 v40, v37, v41, v40
	v_perm_b32 v41, 0, v73, v170
	v_pk_fma_f16 v36, v37, v41, v36
	v_perm_b32 v37, v45, v45, s63
	s_waitcnt lgkmcnt(2)
	v_perm_b32 v41, 0, v74, v169
	v_pk_fma_f16 v38, v37, v41, v38
	v_perm_b32 v41, 0, v74, v170
	v_pk_fma_f16 v39, v37, v41, v39
	v_perm_b32 v41, 0, v75, v169
	v_pk_fma_f16 v40, v37, v41, v40
	v_perm_b32 v41, 0, v75, v170
	v_pk_fma_f16 v36, v37, v41, v36
	v_perm_b32 v37, v46, v46, s63
	s_waitcnt lgkmcnt(1)
	v_perm_b32 v41, 0, v76, v169
	v_pk_fma_f16 v38, v37, v41, v38
	v_perm_b32 v41, 0, v76, v170
	s_waitcnt vmcnt(18)
	v_bfe_u32 v81, v49, 16, 16
	v_pk_fma_f16 v39, v37, v41, v39
	v_perm_b32 v41, 0, v77, v169
	v_lshl_add_u32 v82, v81, 3, 0
	s_waitcnt vmcnt(17)
	v_bfe_u32 v81, v50, 16, 16
	v_pk_fma_f16 v40, v37, v41, v40
	v_perm_b32 v41, 0, v77, v170
	v_bfe_u32 v80, v48, 16, 16
	v_lshl_add_u32 v84, v81, 3, 0
	s_waitcnt vmcnt(16)
	v_bfe_u32 v81, v51, 16, 16
	v_pk_fma_f16 v36, v37, v41, v36
	v_perm_b32 v37, v47, v47, s63
	s_waitcnt lgkmcnt(0)
	v_perm_b32 v41, 0, v78, v169
	v_lshl_add_u32 v80, v80, 3, 0
	v_lshl_add_u32 v86, v81, 3, 0
	v_pk_fma_f16 v38, v37, v41, v38
	v_perm_b32 v41, 0, v78, v170
	ds_read_b64 v[80:81], v80
	ds_read_b64 v[82:83], v82
	ds_read_b64 v[84:85], v84
	ds_read_b64 v[86:87], v86
	v_pk_fma_f16 v39, v37, v41, v39
	v_perm_b32 v41, 0, v79, v169
	v_pk_fma_f16 v40, v37, v41, v40
	v_perm_b32 v41, 0, v79, v170
	v_pk_fma_f16 v36, v37, v41, v36
	v_perm_b32 v37, v48, v48, s63
	s_waitcnt lgkmcnt(3)
	v_perm_b32 v41, 0, v80, v169
	v_pk_fma_f16 v38, v37, v41, v38
	v_perm_b32 v41, 0, v80, v170
	v_pk_fma_f16 v39, v37, v41, v39
	v_perm_b32 v41, 0, v81, v169
	v_pk_fma_f16 v40, v37, v41, v40
	v_perm_b32 v41, 0, v81, v170
	v_pk_fma_f16 v36, v37, v41, v36
	v_perm_b32 v37, v49, v49, s63
	s_waitcnt lgkmcnt(2)
	v_perm_b32 v41, 0, v82, v169
	v_pk_fma_f16 v38, v37, v41, v38
	v_perm_b32 v41, 0, v82, v170
	v_pk_fma_f16 v39, v37, v41, v39
	v_perm_b32 v41, 0, v83, v169
	v_pk_fma_f16 v40, v37, v41, v40
	v_perm_b32 v41, 0, v83, v170
	v_pk_fma_f16 v36, v37, v41, v36
	v_perm_b32 v37, v50, v50, s63
	s_waitcnt lgkmcnt(1)
	v_perm_b32 v41, 0, v84, v169
	v_pk_fma_f16 v38, v37, v41, v38
	v_perm_b32 v41, 0, v84, v170
	v_pk_fma_f16 v39, v37, v41, v39
	v_perm_b32 v41, 0, v85, v169
	v_pk_fma_f16 v40, v37, v41, v40
	v_perm_b32 v41, 0, v85, v170
	v_pk_fma_f16 v36, v37, v41, v36
	v_perm_b32 v37, v51, v51, s63
	s_waitcnt lgkmcnt(0)
	v_perm_b32 v41, 0, v86, v169
	v_pk_fma_f16 v58, v37, v41, v38
	v_perm_b32 v38, 0, v86, v170
	v_pk_fma_f16 v59, v37, v38, v39
	v_perm_b32 v38, 0, v87, v169
	v_pk_fma_f16 v60, v37, v38, v40
	v_perm_b32 v38, 0, v87, v170
	v_pk_fma_f16 v61, v37, v38, v36
	s_and_b32 s8, s46, 0x60
	s_mul_i32 s8, s8, 0x8040
	s_add_u32 s98, s16, s8
	s_addc_u32 s99, s17, 0
	global_load_dword v36, v238, s[98:99]
	s_add_u32 s78, s98, s62
	s_addc_u32 s79, s99, 0
	global_load_dword v37, v238, s[78:79] offset:64
	s_add_u32 s78, s98, s56
	s_addc_u32 s79, s99, 0
	global_load_dword v38, v238, s[78:79] offset:128
	s_add_u32 s78, s98, s57
	s_addc_u32 s79, s99, 0
	global_load_dword v39, v238, s[78:79] offset:192
	s_add_u32 s78, s98, s64
	s_addc_u32 s79, s99, 0
	global_load_dword v40, v238, s[78:79] offset:256
	s_add_u32 s78, s98, s65
	s_addc_u32 s79, s99, 0
	global_load_dword v41, v238, s[78:79] offset:320
	s_add_u32 s78, s98, s66
	s_addc_u32 s79, s99, 0
	global_load_dword v42, v238, s[78:79] offset:384
	s_add_u32 s78, s98, s67
	s_addc_u32 s79, s99, 0
	global_load_dword v44, v238, s[78:79] offset:448
	s_add_u32 s78, s98, s68
	s_addc_u32 s79, s99, 0
	global_load_dword v43, v238, s[78:79] offset:512
	s_add_u32 s78, s98, s69
	s_addc_u32 s79, s99, 0
	global_load_dword v45, v238, s[78:79] offset:576
	s_add_u32 s78, s98, s70
	s_addc_u32 s79, s99, 0
	global_load_dword v46, v238, s[78:79] offset:640
	s_add_u32 s78, s98, s71
	s_addc_u32 s79, s99, 0
	global_load_dword v47, v238, s[78:79] offset:704
	s_add_u32 s78, s98, s72
	s_addc_u32 s79, s99, 0
	global_load_dword v48, v238, s[78:79] offset:768
	s_add_u32 s78, s98, s73
	s_addc_u32 s79, s99, 0
	global_load_dword v49, v238, s[78:79] offset:832
	s_add_u32 s78, s98, s74
	s_addc_u32 s79, s99, 0
	global_load_dword v50, v238, s[78:79] offset:896
	s_add_u32 s78, s98, s75
	s_addc_u32 s79, s99, 0
	global_load_dword v51, v238, s[78:79] offset:960
	s_waitcnt vmcnt(30)
	v_bfe_u32 v57, v31, 16, 16
	s_waitcnt vmcnt(29)
	v_bfe_u32 v62, v30, 16, 16
	s_waitcnt vmcnt(28)
	v_bfe_u32 v63, v29, 16, 16
	s_waitcnt vmcnt(27)
	v_bfe_u32 v64, v28, 16, 16
	v_perm_b32 v85, v31, v31, s63
	v_perm_b32 v86, v30, v30, s63
	v_perm_b32 v87, v29, v29, s63
	v_perm_b32 v88, v28, v28, s63
	v_cvt_f32_f16_e32 v28, v60
	v_cvt_f32_f16_sdwa v29, v60 dst_sel:DWORD dst_unused:UNUSED_PAD src0_sel:WORD_1
	v_cvt_f32_f16_e32 v30, v61
	v_cvt_f32_f16_sdwa v31, v61 dst_sel:DWORD dst_unused:UNUSED_PAD src0_sel:WORD_1
	v_bfe_u32 v56, v24, 16, 16
	s_waitcnt vmcnt(26)
	v_bfe_u32 v65, v27, 16, 16
	s_waitcnt vmcnt(25)
	v_bfe_u32 v66, v26, 16, 16
	s_waitcnt vmcnt(24)
	v_bfe_u32 v67, v25, 16, 16
	s_waitcnt vmcnt(23)
	v_bfe_u32 v68, v54, 16, 16
	s_waitcnt vmcnt(22)
	v_bfe_u32 v69, v53, 16, 16
	s_waitcnt vmcnt(21)
	v_bfe_u32 v70, v52, 16, 16
	s_waitcnt vmcnt(20)
	v_bfe_u32 v71, v35, 16, 16
	s_waitcnt vmcnt(19)
	v_bfe_u32 v72, v34, 16, 16
	s_waitcnt vmcnt(18)
	v_bfe_u32 v73, v33, 16, 16
	s_waitcnt vmcnt(17)
	v_bfe_u32 v74, v32, 16, 16
	s_waitcnt vmcnt(16)
	v_bfe_u32 v75, v55, 16, 16
	v_perm_b32 v84, v24, v24, s63
	v_perm_b32 v91, v25, v25, s63
	v_perm_b32 v92, v54, v54, s63
	v_perm_b32 v94, v52, v52, s63
	v_perm_b32 v96, v34, v34, s63
	v_perm_b32 v98, v32, v32, s63
	v_cvt_f32_f16_e32 v24, v58
	v_cvt_f32_f16_sdwa v25, v58 dst_sel:DWORD dst_unused:UNUSED_PAD src0_sel:WORD_1
	v_lshl_add_u32 v32, v56, 3, 0
	v_lshl_add_u32 v34, v57, 3, 0
	v_lshl_add_u32 v52, v62, 3, 0
	v_lshl_add_u32 v54, v63, 3, 0
	v_lshl_add_u32 v56, v64, 3, 0
	v_lshl_add_u32 v58, v65, 3, 0
	v_lshl_add_u32 v60, v66, 3, 0
	v_lshl_add_u32 v62, v67, 3, 0
	v_lshl_add_u32 v64, v68, 3, 0
	v_lshl_add_u32 v66, v69, 3, 0
	v_lshl_add_u32 v68, v70, 3, 0
	v_lshl_add_u32 v70, v71, 3, 0
	v_lshl_add_u32 v72, v72, 3, 0
	v_lshl_add_u32 v76, v73, 3, 0
	v_lshl_add_u32 v77, v74, 3, 0
	v_lshl_add_u32 v78, v75, 3, 0
	v_perm_b32 v89, v27, v27, s63
	v_perm_b32 v90, v26, v26, s63
	v_perm_b32 v93, v53, v53, s63
	v_perm_b32 v95, v35, v35, s63
	v_perm_b32 v97, v33, v33, s63
	v_perm_b32 v99, v55, v55, s63
	v_cvt_f32_f16_e32 v26, v59
	v_cvt_f32_f16_sdwa v27, v59 dst_sel:DWORD dst_unused:UNUSED_PAD src0_sel:WORD_1
	ds_read_b64 v[32:33], v32
	ds_read_b64 v[34:35], v34
	ds_read_b64 v[52:53], v52
	ds_read_b64 v[54:55], v54
	ds_read_b64 v[56:57], v56
	ds_read_b64 v[58:59], v58
	ds_read_b64 v[60:61], v60
	ds_read_b64 v[62:63], v62
	ds_read_b64 v[64:65], v64
	ds_read_b64 v[66:67], v66
	ds_read_b64 v[68:69], v68
	ds_read_b64 v[70:71], v70
	ds_read_b64 v[72:73], v72
	ds_read_b64 v[74:75], v76
	ds_read_b64 v[76:77], v77
	ds_read_b64 v[78:79], v78
	v_pk_add_f32 v[22:23], v[22:23], v[28:29]
	v_pk_add_f32 v[20:21], v[20:21], v[30:31]
	s_waitcnt lgkmcnt(14)
	v_perm_b32 v28, 0, v32, v169
	v_perm_b32 v29, 0, v32, v170
	v_perm_b32 v30, 0, v33, v169
	v_perm_b32 v31, 0, v33, v170
	v_perm_b32 v32, 0, v34, v169
	v_perm_b32 v33, 0, v34, v170
	v_perm_b32 v34, 0, v35, v169
	v_perm_b32 v35, 0, v35, v170
	v_pk_fma_f16 v28, v84, v28, 0
	v_pk_fma_f16 v29, v84, v29, 0
	v_pk_fma_f16 v30, v84, v30, 0
	v_pk_fma_f16 v31, v84, v31, 0
	s_waitcnt lgkmcnt(13)
	v_perm_b32 v100, 0, v52, v169
	v_perm_b32 v52, 0, v52, v170
	v_perm_b32 v101, 0, v53, v169
	v_perm_b32 v53, 0, v53, v170
	v_pk_fma_f16 v28, v85, v32, v28
	v_pk_fma_f16 v29, v85, v33, v29
	v_pk_fma_f16 v30, v85, v34, v30
	v_pk_fma_f16 v31, v85, v35, v31
	s_waitcnt lgkmcnt(12)
	v_perm_b32 v102, 0, v54, v169
	v_perm_b32 v54, 0, v54, v170
	v_perm_b32 v103, 0, v55, v169
	v_perm_b32 v55, 0, v55, v170
	v_pk_fma_f16 v28, v86, v100, v28
	v_pk_fma_f16 v29, v86, v52, v29
	v_pk_fma_f16 v30, v86, v101, v30
	v_pk_fma_f16 v31, v86, v53, v31
	s_waitcnt lgkmcnt(11)
	v_perm_b32 v104, 0, v56, v169
	v_perm_b32 v56, 0, v56, v170
	v_perm_b32 v105, 0, v57, v169
	v_perm_b32 v57, 0, v57, v170
	v_pk_fma_f16 v28, v87, v102, v28
	v_pk_fma_f16 v29, v87, v54, v29
	v_pk_fma_f16 v30, v87, v103, v30
	v_pk_fma_f16 v31, v87, v55, v31
	s_waitcnt lgkmcnt(10)
	v_perm_b32 v106, 0, v58, v169
	v_perm_b32 v58, 0, v58, v170
	v_perm_b32 v107, 0, v59, v169
	v_perm_b32 v59, 0, v59, v170
	v_pk_fma_f16 v28, v88, v104, v28
	v_pk_fma_f16 v29, v88, v56, v29
	v_pk_fma_f16 v30, v88, v105, v30
	v_pk_fma_f16 v31, v88, v57, v31
	s_waitcnt lgkmcnt(9)
; #define VL_LOAD(wr, C) do { _Pragma("unroll") for (int i = 0; i < 16; ++i) wr[i] = wp[(size_t)((C) * 16 + i) * MROWS]; } while (0)
; #define VL_LOAD(wr, C) do { _Pragma("unroll") for (int i = 0; i < 16; ++i) wr[i] = wp[(size_t)((C) * 16 + i) * MROWS]; } while (0)
; template <bool RUN_L = true, bool RUN_G = true, bool DRY = false>
; __device__ __forceinline__ void phase_vaccH(unsigned char* ws, LAS unsigned char* lds, int layer, int G) {
;     ...
;                 VL_LOAD(wa, 0);
; #pragma unroll 1
;                 for (int c = 0; c < 8; c += 2) {
;                     VL_LOAD(wb, c + 1);
;                     __builtin_amdgcn_sched_barrier(0);
;                     VL_CHUNK(wa);
;                     __builtin_amdgcn_sched_barrier(0);
;                     VL_LOAD(wa, (c + 2) & 7);
;                     __builtin_amdgcn_sched_barrier(0);
;                     VL_CHUNK(wb);
;                     __builtin_amdgcn_sched_barrier(0);
;                 }
;                 if (valid) { hp[0] = h0 + (f32x4){accf[0], accf[1], accf[2], accf[3]}; hp[1] = h1 + (f32x4){accf[4], accf[5], accf[6], accf[7]}; }
	v_perm_b32 v108, 0, v60, v169
	v_perm_b32 v60, 0, v60, v170
	v_perm_b32 v109, 0, v61, v169
	v_perm_b32 v61, 0, v61, v170
	v_pk_fma_f16 v28, v89, v106, v28
	v_pk_fma_f16 v29, v89, v58, v29
	v_pk_fma_f16 v30, v89, v107, v30
	v_pk_fma_f16 v31, v89, v59, v31
	s_waitcnt lgkmcnt(8)
	v_perm_b32 v110, 0, v62, v169
	v_perm_b32 v62, 0, v62, v170
	v_perm_b32 v111, 0, v63, v169
	v_perm_b32 v63, 0, v63, v170
	v_pk_fma_f16 v28, v90, v108, v28
	v_pk_fma_f16 v29, v90, v60, v29
	v_pk_fma_f16 v30, v90, v109, v30
	v_pk_fma_f16 v31, v90, v61, v31
	s_waitcnt lgkmcnt(7)
	v_perm_b32 v112, 0, v64, v169
	v_perm_b32 v64, 0, v64, v170
	v_perm_b32 v113, 0, v65, v169
	v_perm_b32 v65, 0, v65, v170
	v_pk_fma_f16 v28, v91, v110, v28
	v_pk_fma_f16 v29, v91, v62, v29
	v_pk_fma_f16 v30, v91, v111, v30
	v_pk_fma_f16 v31, v91, v63, v31
	s_waitcnt lgkmcnt(6)
	v_perm_b32 v114, 0, v66, v169
	v_perm_b32 v66, 0, v66, v170
	v_perm_b32 v115, 0, v67, v169
	v_perm_b32 v67, 0, v67, v170
	v_pk_fma_f16 v28, v92, v112, v28
	v_pk_fma_f16 v29, v92, v64, v29
	v_pk_fma_f16 v30, v92, v113, v30
	v_pk_fma_f16 v31, v92, v65, v31
	s_waitcnt lgkmcnt(5)
	v_perm_b32 v116, 0, v68, v169
	v_perm_b32 v68, 0, v68, v170
	v_perm_b32 v117, 0, v69, v169
	v_perm_b32 v69, 0, v69, v170
	v_pk_fma_f16 v28, v93, v114, v28
	v_pk_fma_f16 v29, v93, v66, v29
	v_pk_fma_f16 v30, v93, v115, v30
	v_pk_fma_f16 v31, v93, v67, v31
	s_waitcnt lgkmcnt(4)
	v_perm_b32 v118, 0, v70, v169
	v_perm_b32 v70, 0, v70, v170
	v_perm_b32 v119, 0, v71, v169
	v_perm_b32 v71, 0, v71, v170
	v_pk_fma_f16 v28, v94, v116, v28
	v_pk_fma_f16 v29, v94, v68, v29
	v_pk_fma_f16 v30, v94, v117, v30
	v_pk_fma_f16 v31, v94, v69, v31
	s_waitcnt lgkmcnt(3)
	v_perm_b32 v120, 0, v72, v169
	v_perm_b32 v72, 0, v72, v170
	v_perm_b32 v121, 0, v73, v169
	v_perm_b32 v73, 0, v73, v170
	v_pk_fma_f16 v28, v95, v118, v28
	v_pk_fma_f16 v29, v95, v70, v29
	v_pk_fma_f16 v30, v95, v119, v30
	v_pk_fma_f16 v31, v95, v71, v31
	s_waitcnt lgkmcnt(2)
	v_perm_b32 v122, 0, v74, v169
	v_perm_b32 v74, 0, v74, v170
	v_perm_b32 v123, 0, v75, v169
	v_perm_b32 v75, 0, v75, v170
	v_pk_fma_f16 v28, v96, v120, v28
	v_pk_fma_f16 v29, v96, v72, v29
	v_pk_fma_f16 v30, v96, v121, v30
	v_pk_fma_f16 v31, v96, v73, v31
	s_waitcnt lgkmcnt(1)
	v_perm_b32 v124, 0, v76, v169
	v_perm_b32 v76, 0, v76, v170
	v_perm_b32 v125, 0, v77, v169
	v_perm_b32 v77, 0, v77, v170
	v_pk_fma_f16 v28, v97, v122, v28
	v_pk_fma_f16 v29, v97, v74, v29
	v_pk_fma_f16 v30, v97, v123, v30
	v_pk_fma_f16 v31, v97, v75, v31
	s_waitcnt lgkmcnt(0)
	v_perm_b32 v126, 0, v78, v169
	v_perm_b32 v78, 0, v78, v170
	v_perm_b32 v127, 0, v79, v169
	v_perm_b32 v79, 0, v79, v170
	v_pk_fma_f16 v28, v98, v124, v28
	v_pk_fma_f16 v29, v98, v76, v29
	v_pk_fma_f16 v30, v98, v125, v30
	v_pk_fma_f16 v31, v98, v77, v31
	v_pk_fma_f16 v33, v99, v126, v28
	v_pk_fma_f16 v52, v99, v78, v29
	v_pk_fma_f16 v29, v99, v127, v30
	v_pk_fma_f16 v31, v99, v79, v31
	v_cvt_f32_f16_e32 v32, v33
	v_cvt_f32_f16_e32 v30, v52
	v_cvt_f32_f16_e32 v28, v29
	v_cvt_f32_f16_e32 v34, v31
	v_cvt_f32_f16_sdwa v35, v31 dst_sel:DWORD dst_unused:UNUSED_PAD src0_sel:WORD_1
	v_cvt_f32_f16_sdwa v29, v29 dst_sel:DWORD dst_unused:UNUSED_PAD src0_sel:WORD_1
	v_cvt_f32_f16_sdwa v31, v52 dst_sel:DWORD dst_unused:UNUSED_PAD src0_sel:WORD_1
	v_cvt_f32_f16_sdwa v33, v33 dst_sel:DWORD dst_unused:UNUSED_PAD src0_sel:WORD_1
	v_pk_add_f32 v[80:81], v[18:19], v[24:25]
	v_pk_add_f32 v[82:83], v[16:17], v[26:27]
	v_pk_add_f32 v[20:21], v[20:21], v[34:35]
	v_pk_add_f32 v[22:23], v[22:23], v[28:29]
	v_pk_add_f32 v[34:35], v[82:83], v[30:31]
	v_pk_add_f32 v[28:29], v[80:81], v[32:33]
	s_add_u32 s76, s76, s20
	s_addc_u32 s77, s77, s21
	s_add_i32 s46, s46, 32
	s_add_i32 s47, s47, 2
	s_cmp_lt_u32 s47, 6
	v_lshl_add_u64 v[14:15], v[14:15], 0, s[20:21]
	s_cbranch_scc1 .LBB0_1242
	s_and_saveexec_b64 s[46:47], s[6:7]
	s_cbranch_execz .LBB0_1240
	v_pk_add_f32 v[12:13], v[18:19], v[24:25]
	v_pk_add_f32 v[14:15], v[16:17], v[26:27]
	v_pk_add_f32 v[12:13], v[12:13], v[32:33]
	v_pk_add_f32 v[14:15], v[14:15], v[30:31]
	v_pk_add_f32 v[6:7], v[6:7], v[12:13]
	v_pk_add_f32 v[8:9], v[8:9], v[14:15]
	v_pk_add_f32 v[4:5], v[4:5], v[20:21]
	v_pk_add_f32 v[2:3], v[2:3], v[22:23]
	global_store_dwordx4 v[10:11], v[6:9], off
	global_store_dwordx4 v[10:11], v[2:5], off offset:16
	s_branch .LBB0_1240

; #define VL_LOAD(wr, C) do { _Pragma("unroll") for (int i = 0; i < 16; ++i) wr[i] = wp[(size_t)((C) * 16 + i) * MROWS]; } while (0)
; #define VL_LOAD(wr, C) do { _Pragma("unroll") for (int i = 0; i < 16; ++i) wr[i] = wp[(size_t)((C) * 16 + i) * MROWS]; } while (0)
; template <bool RUN_L = true, bool RUN_G = true, bool DRY = false>
; __device__ __forceinline__ void phase_vaccH(unsigned char* ws, LAS unsigned char* lds, int layer, int G) {
;     ...
;             for (int tb = wid; tb < NTB; tb += 4) {
;                 const int tok = tb * 64 + lane; const bool valid = tok < MROWS; const int tokc = valid ? tok : MROWS - 1;
;                 const unsigned* wp = WLT + tokc;
;                 f32x4* hp = (f32x4*)(H + (size_t)tokc * D + cg * 8); const f32x4 h0 = hp[0], h1 = hp[1];
;                 float accf[8];
; #pragma unroll
;                 for (int j = 0; j < 8; ++j) accf[j] = 0.f;
;                 unsigned wa[16], wb[16];
;                 VL_LOAD(wa, 0);
; #pragma unroll 1
;                 for (int c = 0; c < 8; c += 2) {
;                     VL_LOAD(wb, c + 1);
.LBB0_1986:
	s_waitcnt vmcnt(1)
	v_lshl_or_b32 v2, s23, 6, v1
	v_cmp_gt_i32_e64 s[6:7], s39, v2
	s_mov_b32 s30, 32
	s_mov_b32 s31, -2
	v_cndmask_b32_e64 v12, v171, v2, s[6:7]
	v_ashrrev_i32_e32 v13, 31, v12
	v_lshlrev_b64 v[14:15], 2, v[12:13]
	v_mov_b32_e32 v238, v14
	v_lshlrev_b64 v[2:3], 14, v[12:13]
	v_lshl_add_u64 v[12:13], s[16:17], 0, v[14:15]
	v_lshl_add_u64 v[10:11], s[28:29], 0, v[2:3]
	global_load_dwordx4 v[2:5], v[10:11], off offset:16
	global_load_dwordx4 v[6:9], v[10:11], off
	v_lshl_add_u64 v[14:15], s[18:19], 0, v[14:15]
	s_mov_b64 s[76:77], s[18:19]
	global_load_dword v46, v238, s[16:17]
	s_add_u32 s78, s16, s52
	s_addc_u32 s79, s17, 0
	global_load_dword v44, v238, s[78:79] offset:64
	s_add_u32 s78, s16, s41
	s_addc_u32 s79, s17, 0
	global_load_dword v42, v238, s[78:79] offset:128
	s_add_u32 s78, s16, s45
	s_addc_u32 s79, s17, 0
	global_load_dword v40, v238, s[78:79] offset:192
	s_add_u32 s78, s16, s54
	s_addc_u32 s79, s17, 0
	global_load_dword v39, v238, s[78:79] offset:256
	s_add_u32 s78, s16, s55
	s_addc_u32 s79, s17, 0
	global_load_dword v38, v238, s[78:79] offset:320
	s_add_u32 s78, s16, s56
	s_addc_u32 s79, s17, 0
	global_load_dword v37, v238, s[78:79] offset:384
	s_add_u32 s78, s16, s57
	s_addc_u32 s79, s17, 0
	global_load_dword v36, v238, s[78:79] offset:448
	s_add_u32 s78, s16, s58
	s_addc_u32 s79, s17, 0
	global_load_dword v51, v238, s[78:79] offset:512
	s_add_u32 s78, s16, s59
	s_addc_u32 s79, s17, 0
	global_load_dword v50, v238, s[78:79] offset:576
	s_add_u32 s78, s16, s60
	s_addc_u32 s79, s17, 0
	global_load_dword v49, v238, s[78:79] offset:640
	s_add_u32 s78, s16, s61
	s_addc_u32 s79, s17, 0
	global_load_dword v48, v238, s[78:79] offset:704
	s_add_u32 s78, s16, s62
	s_addc_u32 s79, s17, 0
	global_load_dword v47, v238, s[78:79] offset:768
	s_add_u32 s78, s16, 0x68000
	s_addc_u32 s79, s17, 0
	global_load_dword v45, v238, s[78:79] offset:832
	s_add_u32 s78, s16, 0x70000
	s_addc_u32 s79, s17, 0
	global_load_dword v43, v238, s[78:79] offset:896
	s_add_u32 s78, s16, 0x78000
	s_addc_u32 s79, s17, 0
	global_load_dword v41, v238, s[78:79] offset:960
	v_mov_b32_e32 v28, 0
	v_mov_b32_e32 v29, v28
	v_mov_b32_e32 v30, v28
	v_mov_b32_e32 v31, v28
	v_mov_b32_e32 v22, v28
	v_mov_b32_e32 v23, v28
	v_mov_b32_e32 v20, v28
	v_mov_b32_e32 v21, v28
.LBB0_1987:
	s_add_u32 s78, s76, s52
	s_addc_u32 s79, s77, 0
	global_load_dword v72, v238, s[78:79] offset:64
	s_add_u32 s78, s76, s41
	s_addc_u32 s79, s77, 0
	global_load_dword v73, v238, s[78:79] offset:128
	s_add_u32 s78, s76, s45
	s_addc_u32 s79, s77, 0
	global_load_dword v74, v238, s[78:79] offset:192
	s_add_u32 s78, s76, s54
	s_addc_u32 s79, s77, 0
	global_load_dword v75, v238, s[78:79] offset:256
	s_add_u32 s78, s76, s55
	s_addc_u32 s79, s77, 0
	global_load_dword v76, v238, s[78:79] offset:320
	s_add_u32 s78, s76, s56
	s_addc_u32 s79, s77, 0
	global_load_dword v77, v238, s[78:79] offset:384
	s_add_u32 s78, s76, s57
	s_addc_u32 s79, s77, 0
	global_load_dword v78, v238, s[78:79] offset:448
	s_add_u32 s78, s76, s58
	s_addc_u32 s79, s77, 0
	global_load_dword v79, v238, s[78:79] offset:512
	global_load_dword v80, v238, s[76:77]
	s_add_u32 s78, s76, s59
	s_addc_u32 s79, s77, 0
	global_load_dword v81, v238, s[78:79] offset:576
	s_add_u32 s78, s76, s60
	s_addc_u32 s79, s77, 0
	global_load_dword v82, v238, s[78:79] offset:640
	s_add_u32 s78, s76, s61
	s_addc_u32 s79, s77, 0
	global_load_dword v83, v238, s[78:79] offset:704
	s_add_u32 s78, s76, s62
	s_addc_u32 s79, s77, 0
	global_load_dword v84, v238, s[78:79] offset:768
	s_add_u32 s78, s76, s63
	s_addc_u32 s79, s77, 0
	global_load_dword v85, v238, s[78:79] offset:832
	s_add_u32 s78, s76, s64
	s_addc_u32 s79, s77, 0
	global_load_dword v86, v238, s[78:79] offset:896
	s_add_u32 s78, s76, s65
	s_addc_u32 s79, s77, 0
	global_load_dword v87, v238, s[78:79] offset:960
	v_mov_b32_e32 v17, v31
	v_mov_b32_e32 v16, v30
	v_mov_b32_e32 v19, v29
	v_mov_b32_e32 v18, v28
	s_waitcnt vmcnt(30)
	v_bfe_u32 v25, v44, 16, 16
	v_lshl_add_u32 v26, v25, 3, 0
	s_waitcnt vmcnt(29)
	v_bfe_u32 v25, v42, 16, 16
	v_bfe_u32 v24, v46, 16, 16
	v_lshl_add_u32 v28, v25, 3, 0
	s_waitcnt vmcnt(28)
	v_bfe_u32 v25, v40, 16, 16
	v_lshl_add_u32 v24, v24, 3, 0
	v_lshl_add_u32 v30, v25, 3, 0
	ds_read_b64 v[24:25], v24
	ds_read_b64 v[26:27], v26
	ds_read_b64 v[28:29], v28
	ds_read_b64 v[30:31], v30
	v_perm_b32 v46, v46, v46, s53
	s_waitcnt lgkmcnt(3)
	v_perm_b32 v88, 0, v24, v169
	v_perm_b32 v24, 0, v24, v170
	v_perm_b32 v89, 0, v25, v169
	v_perm_b32 v25, 0, v25, v170
	v_pk_fma_f16 v88, v46, v88, 0
	v_pk_fma_f16 v24, v46, v24, 0
	v_pk_fma_f16 v89, v46, v89, 0
	v_pk_fma_f16 v25, v46, v25, 0
	v_perm_b32 v44, v44, v44, s53
	s_waitcnt lgkmcnt(2)
	v_perm_b32 v46, 0, v26, v169
	v_perm_b32 v26, 0, v26, v170
	v_pk_fma_f16 v24, v44, v26, v24
	v_perm_b32 v26, 0, v27, v169
	v_perm_b32 v27, 0, v27, v170
	s_waitcnt vmcnt(26)
	v_bfe_u32 v33, v38, 16, 16
	v_pk_fma_f16 v25, v44, v27, v25
	v_perm_b32 v27, v42, v42, s53
	s_waitcnt lgkmcnt(1)
	v_perm_b32 v42, 0, v28, v169
	v_perm_b32 v28, 0, v28, v170
	v_lshl_add_u32 v34, v33, 3, 0
	s_waitcnt vmcnt(25)
	v_bfe_u32 v33, v37, 16, 16
	v_pk_fma_f16 v26, v44, v26, v89
	v_pk_fma_f16 v24, v27, v28, v24
	v_perm_b32 v28, 0, v29, v169
	v_bfe_u32 v32, v39, 16, 16
	v_lshl_add_u32 v52, v33, 3, 0
	s_waitcnt vmcnt(24)
	v_bfe_u32 v33, v36, 16, 16
	v_pk_fma_f16 v46, v44, v46, v88
	v_pk_fma_f16 v26, v27, v28, v26
	v_perm_b32 v28, 0, v29, v170
	v_lshl_add_u32 v32, v32, 3, 0
	v_lshl_add_u32 v54, v33, 3, 0
	v_pk_fma_f16 v42, v27, v42, v46
	v_pk_fma_f16 v25, v27, v28, v25
	v_perm_b32 v27, v40, v40, s53
	s_waitcnt lgkmcnt(0)
; #define VL_LOAD(wr, C) do { _Pragma("unroll") for (int i = 0; i < 16; ++i) wr[i] = wp[(size_t)((C) * 16 + i) * MROWS]; } while (0)
; #define VL_LOAD(wr, C) do { _Pragma("unroll") for (int i = 0; i < 16; ++i) wr[i] = wp[(size_t)((C) * 16 + i) * MROWS]; } while (0)
; template <bool RUN_L = true, bool RUN_G = true, bool DRY = false>
; __device__ __forceinline__ void phase_vaccH(unsigned char* ws, LAS unsigned char* lds, int layer, int G) {
;     ...
;                     VL_CHUNK(wa);
;                     __builtin_amdgcn_sched_barrier(0);
;                     VL_LOAD(wa, (c + 2) & 7);
	v_perm_b32 v29, 0, v30, v170
	ds_read_b64 v[32:33], v32
	ds_read_b64 v[34:35], v34
	ds_read_b64 v[52:53], v52
	ds_read_b64 v[54:55], v54
	v_pk_fma_f16 v24, v27, v29, v24
	v_perm_b32 v29, 0, v31, v169
	v_perm_b32 v28, 0, v30, v169
	v_pk_fma_f16 v26, v27, v29, v26
	v_perm_b32 v29, 0, v31, v170
	v_pk_fma_f16 v28, v27, v28, v42
	v_pk_fma_f16 v25, v27, v29, v25
	v_perm_b32 v27, v39, v39, s53
	s_waitcnt lgkmcnt(3)
	v_perm_b32 v29, 0, v32, v169
	v_pk_fma_f16 v28, v27, v29, v28
	v_perm_b32 v29, 0, v32, v170
	v_pk_fma_f16 v24, v27, v29, v24
	v_perm_b32 v29, 0, v33, v169
	v_pk_fma_f16 v26, v27, v29, v26
	v_perm_b32 v29, 0, v33, v170
	v_pk_fma_f16 v25, v27, v29, v25
	v_perm_b32 v27, v38, v38, s53
	s_waitcnt lgkmcnt(2)
	v_perm_b32 v29, 0, v34, v169
	v_pk_fma_f16 v28, v27, v29, v28
	v_perm_b32 v29, 0, v34, v170
	v_pk_fma_f16 v24, v27, v29, v24
	v_perm_b32 v29, 0, v35, v169
	v_pk_fma_f16 v26, v27, v29, v26
	v_perm_b32 v29, 0, v35, v170
	v_pk_fma_f16 v25, v27, v29, v25
	v_perm_b32 v27, v37, v37, s53
	s_waitcnt lgkmcnt(1)
	v_perm_b32 v29, 0, v52, v169
	v_pk_fma_f16 v28, v27, v29, v28
	v_perm_b32 v29, 0, v52, v170
	s_waitcnt vmcnt(22)
	v_bfe_u32 v57, v50, 16, 16
	v_pk_fma_f16 v24, v27, v29, v24
	v_perm_b32 v29, 0, v53, v169
	v_lshl_add_u32 v58, v57, 3, 0
	s_waitcnt vmcnt(21)
	v_bfe_u32 v57, v49, 16, 16
	v_pk_fma_f16 v26, v27, v29, v26
	v_perm_b32 v29, 0, v53, v170
	v_bfe_u32 v56, v51, 16, 16
	v_lshl_add_u32 v60, v57, 3, 0
	s_waitcnt vmcnt(20)
	v_bfe_u32 v57, v48, 16, 16
	v_pk_fma_f16 v25, v27, v29, v25
	v_perm_b32 v27, v36, v36, s53
	s_waitcnt lgkmcnt(0)
	v_perm_b32 v29, 0, v54, v169
	v_lshl_add_u32 v56, v56, 3, 0
	v_lshl_add_u32 v62, v57, 3, 0
	v_pk_fma_f16 v28, v27, v29, v28
	v_perm_b32 v29, 0, v54, v170
	ds_read_b64 v[56:57], v56
	ds_read_b64 v[58:59], v58
	ds_read_b64 v[60:61], v60
	ds_read_b64 v[62:63], v62
	v_pk_fma_f16 v24, v27, v29, v24
	v_perm_b32 v29, 0, v55, v169
	v_pk_fma_f16 v26, v27, v29, v26
	v_perm_b32 v29, 0, v55, v170
	v_pk_fma_f16 v25, v27, v29, v25
	v_perm_b32 v27, v51, v51, s53
	s_waitcnt lgkmcnt(3)
	v_perm_b32 v29, 0, v56, v169
	v_pk_fma_f16 v28, v27, v29, v28
	v_perm_b32 v29, 0, v56, v170
	v_pk_fma_f16 v24, v27, v29, v24
	v_perm_b32 v29, 0, v57, v169
	v_pk_fma_f16 v26, v27, v29, v26
	v_perm_b32 v29, 0, v57, v170
	v_pk_fma_f16 v25, v27, v29, v25
	v_perm_b32 v27, v50, v50, s53
	s_waitcnt lgkmcnt(2)
	v_perm_b32 v29, 0, v58, v169
	v_pk_fma_f16 v28, v27, v29, v28
	v_perm_b32 v29, 0, v58, v170
	v_pk_fma_f16 v24, v27, v29, v24
	v_perm_b32 v29, 0, v59, v169
	v_pk_fma_f16 v26, v27, v29, v26
	v_perm_b32 v29, 0, v59, v170
	v_pk_fma_f16 v25, v27, v29, v25
	v_perm_b32 v27, v49, v49, s53
	s_waitcnt lgkmcnt(1)
	v_perm_b32 v29, 0, v60, v169
	v_pk_fma_f16 v28, v27, v29, v28
	v_perm_b32 v29, 0, v60, v170
	s_waitcnt vmcnt(18)
	v_bfe_u32 v65, v45, 16, 16
	v_pk_fma_f16 v24, v27, v29, v24
	v_perm_b32 v29, 0, v61, v169
	v_lshl_add_u32 v66, v65, 3, 0
	s_waitcnt vmcnt(17)
	v_bfe_u32 v65, v43, 16, 16
	v_pk_fma_f16 v26, v27, v29, v26
	v_perm_b32 v29, 0, v61, v170
	v_bfe_u32 v64, v47, 16, 16
	v_lshl_add_u32 v68, v65, 3, 0
	s_waitcnt vmcnt(16)
	v_bfe_u32 v65, v41, 16, 16
	v_pk_fma_f16 v25, v27, v29, v25
	v_perm_b32 v27, v48, v48, s53
	s_waitcnt lgkmcnt(0)
	v_perm_b32 v29, 0, v62, v169
	v_lshl_add_u32 v64, v64, 3, 0
	v_lshl_add_u32 v70, v65, 3, 0
	v_pk_fma_f16 v28, v27, v29, v28
	v_perm_b32 v29, 0, v62, v170
	ds_read_b64 v[64:65], v64
	ds_read_b64 v[66:67], v66
	ds_read_b64 v[68:69], v68
	ds_read_b64 v[70:71], v70
	v_pk_fma_f16 v24, v27, v29, v24
	v_perm_b32 v29, 0, v63, v169
	v_pk_fma_f16 v26, v27, v29, v26
	v_perm_b32 v29, 0, v63, v170
	v_pk_fma_f16 v25, v27, v29, v25
	v_perm_b32 v27, v47, v47, s53
	s_waitcnt lgkmcnt(3)
	v_perm_b32 v29, 0, v64, v169
	v_pk_fma_f16 v28, v27, v29, v28
	v_perm_b32 v29, 0, v64, v170
	v_pk_fma_f16 v24, v27, v29, v24
	v_perm_b32 v29, 0, v65, v169
	v_pk_fma_f16 v26, v27, v29, v26
	v_perm_b32 v29, 0, v65, v170
	v_pk_fma_f16 v25, v27, v29, v25
	v_perm_b32 v27, v45, v45, s53
	s_waitcnt lgkmcnt(2)
	v_perm_b32 v29, 0, v66, v169
	v_pk_fma_f16 v28, v27, v29, v28
	v_perm_b32 v29, 0, v66, v170
	v_pk_fma_f16 v24, v27, v29, v24
	v_perm_b32 v29, 0, v67, v169
	v_pk_fma_f16 v26, v27, v29, v26
	v_perm_b32 v29, 0, v67, v170
	v_pk_fma_f16 v25, v27, v29, v25
	v_perm_b32 v27, v43, v43, s53
	s_waitcnt lgkmcnt(1)
	v_perm_b32 v29, 0, v68, v169
	v_pk_fma_f16 v28, v27, v29, v28
	v_perm_b32 v29, 0, v68, v170
	v_pk_fma_f16 v24, v27, v29, v24
	v_perm_b32 v29, 0, v69, v169
	v_pk_fma_f16 v26, v27, v29, v26
	v_perm_b32 v29, 0, v69, v170
	v_pk_fma_f16 v25, v27, v29, v25
	v_perm_b32 v27, v41, v41, s53
	s_waitcnt lgkmcnt(0)
	v_perm_b32 v29, 0, v70, v169
	v_pk_fma_f16 v56, v27, v29, v28
	v_perm_b32 v28, 0, v70, v170
	v_pk_fma_f16 v57, v27, v28, v24
	v_perm_b32 v24, 0, v71, v169
	v_pk_fma_f16 v58, v27, v24, v26
	v_perm_b32 v24, 0, v71, v170
	v_pk_fma_f16 v59, v27, v24, v25
	s_and_b32 s8, s30, 0x60
	s_mul_i32 s8, s8, 0x8040
	s_add_u32 s98, s16, s8
	s_addc_u32 s99, s17, 0
	global_load_dword v46, v238, s[98:99]
	s_add_u32 s78, s98, s52
	s_addc_u32 s79, s99, 0
	global_load_dword v44, v238, s[78:79] offset:64
	s_add_u32 s78, s98, s41
	s_addc_u32 s79, s99, 0
	global_load_dword v42, v238, s[78:79] offset:128
	s_add_u32 s78, s98, s45
	s_addc_u32 s79, s99, 0
	global_load_dword v40, v238, s[78:79] offset:192
	s_add_u32 s78, s98, s54
	s_addc_u32 s79, s99, 0
	global_load_dword v39, v238, s[78:79] offset:256
	s_add_u32 s78, s98, s55
	s_addc_u32 s79, s99, 0
	global_load_dword v38, v238, s[78:79] offset:320
	s_add_u32 s78, s98, s56
	s_addc_u32 s79, s99, 0
	global_load_dword v37, v238, s[78:79] offset:384
	s_add_u32 s78, s98, s57
	s_addc_u32 s79, s99, 0
	global_load_dword v36, v238, s[78:79] offset:448
	s_add_u32 s78, s98, s58
	s_addc_u32 s79, s99, 0
	global_load_dword v51, v238, s[78:79] offset:512
	s_add_u32 s78, s98, s59
	s_addc_u32 s79, s99, 0
	global_load_dword v50, v238, s[78:79] offset:576
	s_add_u32 s78, s98, s60
	s_addc_u32 s79, s99, 0
	global_load_dword v49, v238, s[78:79] offset:640
	s_add_u32 s78, s98, s61
	s_addc_u32 s79, s99, 0
	global_load_dword v48, v238, s[78:79] offset:704
	s_add_u32 s78, s98, s62
	s_addc_u32 s79, s99, 0
	global_load_dword v47, v238, s[78:79] offset:768
	s_add_u32 s78, s98, s63
	s_addc_u32 s79, s99, 0
	global_load_dword v45, v238, s[78:79] offset:832
	s_add_u32 s78, s98, s64
	s_addc_u32 s79, s99, 0
	global_load_dword v43, v238, s[78:79] offset:896
	s_add_u32 s78, s98, s65
	s_addc_u32 s79, s99, 0
	global_load_dword v41, v238, s[78:79] offset:960
	v_cvt_f32_f16_e32 v28, v58
	v_cvt_f32_f16_sdwa v29, v58 dst_sel:DWORD dst_unused:UNUSED_PAD src0_sel:WORD_1
	v_cvt_f32_f16_e32 v30, v59
	v_cvt_f32_f16_sdwa v31, v59 dst_sel:DWORD dst_unused:UNUSED_PAD src0_sel:WORD_1
	s_waitcnt vmcnt(23)
	v_bfe_u32 v32, v80, 16, 16
	v_bfe_u32 v33, v72, 16, 16
	v_bfe_u32 v34, v73, 16, 16
	v_bfe_u32 v35, v74, 16, 16
	v_bfe_u32 v52, v75, 16, 16
	v_bfe_u32 v53, v76, 16, 16
	v_bfe_u32 v54, v77, 16, 16
	v_bfe_u32 v55, v78, 16, 16
	v_bfe_u32 v60, v79, 16, 16
	s_waitcnt vmcnt(22)
	v_bfe_u32 v61, v81, 16, 16
	s_waitcnt vmcnt(21)
	v_bfe_u32 v62, v82, 16, 16
	s_waitcnt vmcnt(20)
	v_bfe_u32 v63, v83, 16, 16
	s_waitcnt vmcnt(19)
	v_bfe_u32 v64, v84, 16, 16
	s_waitcnt vmcnt(18)
	v_bfe_u32 v65, v85, 16, 16
	s_waitcnt vmcnt(17)
	v_bfe_u32 v66, v86, 16, 16
	s_waitcnt vmcnt(16)
	v_bfe_u32 v67, v87, 16, 16
	v_perm_b32 v89, v72, v72, s53
	v_perm_b32 v90, v73, v73, s53
	v_perm_b32 v91, v74, v74, s53
	v_perm_b32 v92, v75, v75, s53
	v_perm_b32 v93, v76, v76, s53
	v_perm_b32 v94, v77, v77, s53
	v_perm_b32 v95, v78, v78, s53
	v_cvt_f32_f16_e32 v24, v56
	v_cvt_f32_f16_sdwa v25, v56 dst_sel:DWORD dst_unused:UNUSED_PAD src0_sel:WORD_1
	v_cvt_f32_f16_e32 v26, v57
	v_cvt_f32_f16_sdwa v27, v57 dst_sel:DWORD dst_unused:UNUSED_PAD src0_sel:WORD_1
	v_lshl_add_u32 v32, v32, 3, 0
	v_lshl_add_u32 v56, v33, 3, 0
	v_lshl_add_u32 v57, v34, 3, 0
	v_lshl_add_u32 v58, v35, 3, 0
	v_lshl_add_u32 v59, v52, 3, 0
	v_lshl_add_u32 v68, v53, 3, 0
	v_lshl_add_u32 v69, v54, 3, 0
	v_lshl_add_u32 v70, v55, 3, 0
	v_lshl_add_u32 v71, v60, 3, 0
	v_lshl_add_u32 v72, v61, 3, 0
	v_lshl_add_u32 v73, v62, 3, 0
	v_lshl_add_u32 v74, v63, 3, 0
	v_lshl_add_u32 v75, v64, 3, 0
	v_lshl_add_u32 v76, v65, 3, 0
	v_lshl_add_u32 v77, v66, 3, 0
	v_lshl_add_u32 v78, v67, 3, 0
	v_perm_b32 v88, v80, v80, s53
	v_perm_b32 v96, v79, v79, s53
	ds_read_b64 v[32:33], v32
	ds_read_b64 v[34:35], v56
	ds_read_b64 v[52:53], v57
	ds_read_b64 v[54:55], v58
	ds_read_b64 v[56:57], v59
	ds_read_b64 v[58:59], v68
	ds_read_b64 v[60:61], v69
	ds_read_b64 v[62:63], v70
	ds_read_b64 v[64:65], v71
	ds_read_b64 v[66:67], v72
	ds_read_b64 v[68:69], v73
	ds_read_b64 v[70:71], v74
	ds_read_b64 v[72:73], v75
	ds_read_b64 v[74:75], v76
	ds_read_b64 v[76:77], v77
	ds_read_b64 v[78:79], v78
	v_pk_add_f32 v[22:23], v[22:23], v[28:29]
	v_pk_add_f32 v[20:21], v[20:21], v[30:31]
	s_waitcnt lgkmcnt(14)
	v_perm_b32 v28, 0, v32, v169
	v_perm_b32 v29, 0, v32, v170
	v_perm_b32 v30, 0, v33, v169
	v_perm_b32 v31, 0, v33, v170
	v_perm_b32 v32, 0, v34, v169
	v_perm_b32 v33, 0, v34, v170
	v_perm_b32 v34, 0, v35, v169
	v_perm_b32 v35, 0, v35, v170
	v_pk_fma_f16 v28, v88, v28, 0
	v_pk_fma_f16 v29, v88, v29, 0
	v_pk_fma_f16 v30, v88, v30, 0
	v_pk_fma_f16 v31, v88, v31, 0
	s_waitcnt lgkmcnt(13)
	v_perm_b32 v100, 0, v52, v169
	v_perm_b32 v52, 0, v52, v170
	v_perm_b32 v101, 0, v53, v169
	v_perm_b32 v53, 0, v53, v170
	v_pk_fma_f16 v28, v89, v32, v28
	v_pk_fma_f16 v29, v89, v33, v29
	v_pk_fma_f16 v30, v89, v34, v30
	v_pk_fma_f16 v31, v89, v35, v31
	s_waitcnt lgkmcnt(12)
	v_perm_b32 v102, 0, v54, v169
	v_perm_b32 v54, 0, v54, v170
	v_perm_b32 v103, 0, v55, v169
	v_perm_b32 v55, 0, v55, v170
	v_pk_fma_f16 v28, v90, v100, v28
	v_pk_fma_f16 v29, v90, v52, v29
	v_pk_fma_f16 v30, v90, v101, v30
	v_pk_fma_f16 v31, v90, v53, v31
	s_waitcnt lgkmcnt(11)
	v_perm_b32 v104, 0, v56, v169
	v_perm_b32 v56, 0, v56, v170
	v_perm_b32 v105, 0, v57, v169
	v_perm_b32 v57, 0, v57, v170
	v_pk_fma_f16 v28, v91, v102, v28
	v_pk_fma_f16 v29, v91, v54, v29
	v_pk_fma_f16 v30, v91, v103, v30
	v_pk_fma_f16 v31, v91, v55, v31
	s_waitcnt lgkmcnt(10)
	v_perm_b32 v106, 0, v58, v169
	v_perm_b32 v58, 0, v58, v170
	v_perm_b32 v107, 0, v59, v169
	v_perm_b32 v59, 0, v59, v170
	v_pk_fma_f16 v28, v92, v104, v28
	v_pk_fma_f16 v29, v92, v56, v29
	v_pk_fma_f16 v30, v92, v105, v30
	v_pk_fma_f16 v31, v92, v57, v31
	s_waitcnt lgkmcnt(9)
	v_perm_b32 v108, 0, v60, v169
	v_perm_b32 v60, 0, v60, v170
	v_perm_b32 v109, 0, v61, v169
	v_perm_b32 v61, 0, v61, v170
	v_pk_fma_f16 v28, v93, v106, v28
	v_pk_fma_f16 v29, v93, v58, v29
	v_pk_fma_f16 v30, v93, v107, v30
	v_pk_fma_f16 v31, v93, v59, v31
	s_waitcnt lgkmcnt(8)
	v_perm_b32 v110, 0, v62, v169
	v_perm_b32 v62, 0, v62, v170
	v_perm_b32 v111, 0, v63, v169
	v_perm_b32 v63, 0, v63, v170
	v_pk_fma_f16 v28, v94, v108, v28
	v_pk_fma_f16 v29, v94, v60, v29
	v_pk_fma_f16 v30, v94, v109, v30
	v_pk_fma_f16 v31, v94, v61, v31
	s_waitcnt lgkmcnt(7)
; #define VL_LOAD(wr, C) do { _Pragma("unroll") for (int i = 0; i < 16; ++i) wr[i] = wp[(size_t)((C) * 16 + i) * MROWS]; } while (0)
; #define VL_LOAD(wr, C) do { _Pragma("unroll") for (int i = 0; i < 16; ++i) wr[i] = wp[(size_t)((C) * 16 + i) * MROWS]; } while (0)
; template <bool RUN_L = true, bool RUN_G = true, bool DRY = false>
; __device__ __forceinline__ void phase_vaccH(unsigned char* ws, LAS unsigned char* lds, int layer, int G) {
;     ...
;                 VL_LOAD(wa, 0);
; #pragma unroll 1
;                 for (int c = 0; c < 8; c += 2) {
;                     VL_LOAD(wb, c + 1);
;                     __builtin_amdgcn_sched_barrier(0);
;                     VL_CHUNK(wa);
;                     __builtin_amdgcn_sched_barrier(0);
;                     VL_LOAD(wa, (c + 2) & 7);
;                     __builtin_amdgcn_sched_barrier(0);
;                     VL_CHUNK(wb);
;                     __builtin_amdgcn_sched_barrier(0);
;                 }
;                 if (valid) { hp[0] = h0 + (f32x4){accf[0], accf[1], accf[2], accf[3]}; hp[1] = h1 + (f32x4){accf[4], accf[5], accf[6], accf[7]}; }
	v_perm_b32 v112, 0, v64, v169
	v_perm_b32 v64, 0, v64, v170
	v_perm_b32 v113, 0, v65, v169
	v_perm_b32 v65, 0, v65, v170
	v_pk_fma_f16 v28, v95, v110, v28
	v_pk_fma_f16 v29, v95, v62, v29
	v_pk_fma_f16 v30, v95, v111, v30
	v_pk_fma_f16 v31, v95, v63, v31
	v_perm_b32 v97, v81, v81, s53
	s_waitcnt lgkmcnt(6)
	v_perm_b32 v114, 0, v66, v169
	v_perm_b32 v66, 0, v66, v170
	v_perm_b32 v115, 0, v67, v169
	v_perm_b32 v67, 0, v67, v170
	v_pk_fma_f16 v28, v96, v112, v28
	v_pk_fma_f16 v29, v96, v64, v29
	v_pk_fma_f16 v30, v96, v113, v30
	v_pk_fma_f16 v31, v96, v65, v31
	v_perm_b32 v98, v82, v82, s53
	s_waitcnt lgkmcnt(5)
	v_perm_b32 v116, 0, v68, v169
	v_perm_b32 v68, 0, v68, v170
	v_perm_b32 v117, 0, v69, v169
	v_perm_b32 v69, 0, v69, v170
	v_pk_fma_f16 v28, v97, v114, v28
	v_pk_fma_f16 v29, v97, v66, v29
	v_pk_fma_f16 v30, v97, v115, v30
	v_pk_fma_f16 v31, v97, v67, v31
	v_perm_b32 v99, v83, v83, s53
	s_waitcnt lgkmcnt(4)
	v_perm_b32 v118, 0, v70, v169
	v_perm_b32 v70, 0, v70, v170
	v_perm_b32 v119, 0, v71, v169
	v_perm_b32 v71, 0, v71, v170
	v_pk_fma_f16 v28, v98, v116, v28
	v_pk_fma_f16 v29, v98, v68, v29
	v_pk_fma_f16 v30, v98, v117, v30
	v_pk_fma_f16 v31, v98, v69, v31
	v_perm_b32 v84, v84, v84, s53
	s_waitcnt lgkmcnt(3)
	v_perm_b32 v120, 0, v72, v169
	v_perm_b32 v72, 0, v72, v170
	v_perm_b32 v121, 0, v73, v169
	v_perm_b32 v73, 0, v73, v170
	v_pk_fma_f16 v28, v99, v118, v28
	v_pk_fma_f16 v29, v99, v70, v29
	v_pk_fma_f16 v30, v99, v119, v30
	v_pk_fma_f16 v31, v99, v71, v31
	v_perm_b32 v85, v85, v85, s53
	s_waitcnt lgkmcnt(2)
	v_perm_b32 v122, 0, v74, v169
	v_perm_b32 v74, 0, v74, v170
	v_perm_b32 v123, 0, v75, v169
	v_perm_b32 v75, 0, v75, v170
	v_pk_fma_f16 v28, v84, v120, v28
	v_pk_fma_f16 v29, v84, v72, v29
	v_pk_fma_f16 v30, v84, v121, v30
	v_pk_fma_f16 v31, v84, v73, v31
	v_perm_b32 v86, v86, v86, s53
	s_waitcnt lgkmcnt(1)
	v_perm_b32 v124, 0, v76, v169
	v_perm_b32 v76, 0, v76, v170
	v_perm_b32 v125, 0, v77, v169
	v_perm_b32 v77, 0, v77, v170
	v_pk_fma_f16 v28, v85, v122, v28
	v_pk_fma_f16 v29, v85, v74, v29
	v_pk_fma_f16 v30, v85, v123, v30
	v_pk_fma_f16 v31, v85, v75, v31
	v_perm_b32 v87, v87, v87, s53
	s_waitcnt lgkmcnt(0)
	v_perm_b32 v126, 0, v78, v169
	v_perm_b32 v78, 0, v78, v170
	v_perm_b32 v127, 0, v79, v169
	v_perm_b32 v79, 0, v79, v170
	v_pk_fma_f16 v28, v86, v124, v28
	v_pk_fma_f16 v29, v86, v76, v29
	v_pk_fma_f16 v30, v86, v125, v30
	v_pk_fma_f16 v31, v86, v77, v31
	v_pk_fma_f16 v35, v87, v126, v28
	v_pk_fma_f16 v33, v87, v78, v29
	v_pk_fma_f16 v29, v87, v127, v30
	v_pk_fma_f16 v31, v87, v79, v31
	v_cvt_f32_f16_e32 v34, v35
	v_cvt_f32_f16_e32 v32, v33
	v_cvt_f32_f16_e32 v28, v29
	v_cvt_f32_f16_e32 v30, v31
	v_cvt_f32_f16_sdwa v31, v31 dst_sel:DWORD dst_unused:UNUSED_PAD src0_sel:WORD_1
	v_cvt_f32_f16_sdwa v29, v29 dst_sel:DWORD dst_unused:UNUSED_PAD src0_sel:WORD_1
	v_cvt_f32_f16_sdwa v33, v33 dst_sel:DWORD dst_unused:UNUSED_PAD src0_sel:WORD_1
	v_cvt_f32_f16_sdwa v35, v35 dst_sel:DWORD dst_unused:UNUSED_PAD src0_sel:WORD_1
	v_pk_add_f32 v[80:81], v[18:19], v[24:25]
	v_pk_add_f32 v[82:83], v[16:17], v[26:27]
	v_pk_add_f32 v[20:21], v[20:21], v[30:31]
	v_pk_add_f32 v[22:23], v[22:23], v[28:29]
	v_pk_add_f32 v[30:31], v[82:83], v[32:33]
	v_pk_add_f32 v[28:29], v[80:81], v[34:35]
	s_add_u32 s76, s76, s20
	s_addc_u32 s77, s77, s21
	s_add_i32 s30, s30, 32
	s_add_i32 s31, s31, 2
	s_cmp_lt_u32 s31, 6
	v_lshl_add_u64 v[14:15], v[14:15], 0, s[20:21]
	s_cbranch_scc1 .LBB0_1987
	s_and_saveexec_b64 s[30:31], s[6:7]
	s_cbranch_execz .LBB0_1985
	v_pk_add_f32 v[12:13], v[18:19], v[24:25]
	v_pk_add_f32 v[14:15], v[16:17], v[26:27]
	v_pk_add_f32 v[12:13], v[12:13], v[34:35]
	v_pk_add_f32 v[14:15], v[14:15], v[32:33]
	v_pk_add_f32 v[6:7], v[6:7], v[12:13]
	v_pk_add_f32 v[8:9], v[8:9], v[14:15]
	v_pk_add_f32 v[4:5], v[4:5], v[20:21]
	v_pk_add_f32 v[2:3], v[2:3], v[22:23]
	global_store_dwordx4 v[10:11], v[6:9], off
	global_store_dwordx4 v[10:11], v[2:5], off offset:16
	s_branch .LBB0_1985
